# static priority mirrored: one s_setprio 1 for waves 0-3 per GEMM phase, all per-segment flips deleted
# speedup vs baseline: 1.0073x; 1.0073x over previous
; #define PG8_STAGE(bufoff, gbase, voff) do { _Pragma("unroll") for (int _i = 0; _i < 2; ++_i) \
;         __builtin_amdgcn_global_load_lds((const unsigned*)((const char*)(gbase) + (voff)[_i]), (PG8_LAS unsigned*)(lds + (bufoff) + ldsw + _i * 8192), 16, 0, 0); } while (0)
; #define PG8_LDA(dst, b, h) do { _Pragma("unroll") for (int m = 0; m < 4; ++m) _Pragma("unroll") for (int k = 0; k < 2; ++k) dst[m][k] = *(const PG8_LAS bf16x8*)(lds + PG8_SA(b, h) + aoff + m * 2048 + k * 1024); } while (0)
; #define PG8_LDB(dst, b, h) do { _Pragma("unroll") for (int n = 0; n < 2; ++n) _Pragma("unroll") for (int k = 0; k < 2; ++k) dst[n][k] = *(const PG8_LAS bf16x8*)(lds + PG8_SB(b, h) + boff + n * 2048 + k * 1024); } while (0)
; #define PG8_MMA(ai, bj, At, Bt) do { __builtin_amdgcn_s_setprio(1); _Pragma("unroll") for (int m = 0; m < 4; ++m) _Pragma("unroll") for (int n = 0; n < 2; ++n) _Pragma("unroll") for (int k = 0; k < 2; ++k) \
;         acc[ai][bj][m][n] = __builtin_amdgcn_mfma_f32_16x16x32_bf16(Bt[n][k], At[m][k], acc[ai][bj][m][n], 0, 0, 0); __builtin_amdgcn_s_setprio(0); } while (0)
; #define PG8_WAIT_V(n) asm volatile("s_waitcnt vmcnt(" #n ")" ::: "memory")
; #define PG8_WAIT_L(n) asm volatile("s_waitcnt lgkmcnt(" #n ")" ::: "memory")
; #define PG8_BAR __builtin_amdgcn_s_barrier()
; template <class Epi, class Sched, bool ALIGN_EPI>
; __device__ __forceinline__ void gemm_phase(PG8_LAS unsigned char* lds, const Gemm g, const Sched& S, const Epi& E, const int tid) {
;     ...
;         const bool has_next = S.next(ui + 1, nxt);
;         const char* nA = has_next ? (const char*)g.A + (size_t)nxt.pm * tstepA + PG8_ACOL(nxt) : cA; const char* nB = has_next ? (const char*)g.Bt + (size_t)nxt.pn * tstepB : cB;
;         for (int t = 0; t < nt; t += 2) {
;             const bool last = (t == nt - 2);
;             const char* a1 = cA + (size_t)(t + 1) * kstepA;
;             const char* a2 = last ? nA : cA + (size_t)(t + 2) * kstepA; const char* b2 = last ? nB : cB + (size_t)(t + 2) * kstepB;
;             const char* a3 = a2 + kstepA; const char* b3 = b2 + kstepB;
;             if (last && has_next) S.a_ready(nxt);
;             PG8_LDB(B0, 0, 0); PG8_LDB(B1, 0, 1); PG8_SCHED; PG8_LDA(At, 0, 0); PG8_STAGE(PG8_SA(1, 1), a1 + hstepA, voffA);
;             PG8_WAIT_V(8); PG8_WAIT_L(0); PG8_BAR; PG8_MMA(0, 0, At, B0); PG8_MMA(0, 1, At, B1); PG8_BAR; PG8_SCHED;
.LBB0_245:
	s_ashr_i32 s11, s10, 31
	s_lshl_b64 s[12:13], s[10:11], 20
	s_add_u32 s12, s43, s12
	s_addc_u32 s13, s44, s13
	s_and_b64 s[14:15], s[2:3], exec
	s_cselect_b32 s11, s13, s17
	s_cselect_b32 s58, s12, s16
	s_ashr_i32 s9, s8, 31
	s_lshl_b64 s[14:15], s[8:9], 20
	s_add_u32 s14, s40, s14
	s_addc_u32 s15, s41, s15
	s_and_b64 s[20:21], s[2:3], exec
	s_cselect_b32 s9, s15, s19
	s_cselect_b32 s59, s14, s18
	s_add_u32 s16, s16, 0xc000
	s_addc_u32 s17, s17, 0
	s_add_u32 s60, s18, 0x10000
	s_addc_u32 s61, s19, 0
	s_mov_b32 s62, -2
	v_add_u32_e32 v166, 0x10000, v178
	s_add_u32 s18, s16, 0x4000
	s_addc_u32 s19, s17, 0
	s_cmp_eq_u32 s62, 28
	s_cselect_b32 s22, s58, s18
	s_cselect_b32 s23, s11, s19
	s_cselect_b32 s20, s59, s60
	s_cselect_b32 s21, s9, s61
	s_add_u32 s18, s22, 0x8000
	s_addc_u32 s19, s23, 0
	s_add_i32 s63, 0, 0x10000
	s_add_i32 s66, 0, 0x14000
	ds_read_b128 v[80:83], v166
	ds_read_b128 v[84:87], v166 offset:1024
	ds_read_b128 v[96:99], v166 offset:2048
	ds_read_b128 v[100:103], v166 offset:3072
	ds_read_b128 v[162:165], v166 offset:16384
	ds_read_b128 v[182:185], v166 offset:17408
	ds_read_b128 v[186:189], v166 offset:18432
	ds_read_b128 v[190:193], v166 offset:19456
	s_add_i32 m0, s45, 0xc000
	ds_read_b128 v[194:197], v180
	ds_read_b128 v[198:201], v180 offset:1024
	ds_read_b128 v[202:205], v180 offset:2048
	ds_read_b128 v[206:209], v180 offset:3072
	ds_read_b128 v[210:213], v180 offset:4096
	ds_read_b128 v[214:217], v180 offset:5120
	ds_read_b128 v[218:221], v180 offset:6144
	ds_read_b128 v[222:225], v180 offset:7168
	global_load_lds_dwordx4 v158, s[16:17]
	s_add_i32 m0, s45, 0xe000
	s_nop 0
	global_load_lds_dwordx4 v160, s[16:17]
	s_waitcnt vmcnt(8)
	s_waitcnt lgkmcnt(0)
	s_and_b64 vcc, exec, s[6:7]
	s_cbranch_vccz .Lsprio_0
	s_setprio 1

; #define PG8_STAGE(bufoff, gbase, voff) do { _Pragma("unroll") for (int _i = 0; _i < 2; ++_i) \
;         __builtin_amdgcn_global_load_lds((const unsigned*)((const char*)(gbase) + (voff)[_i]), (PG8_LAS unsigned*)(lds + (bufoff) + ldsw + _i * 8192), 16, 0, 0); } while (0)
; #define PG8_LDA(dst, b, h) do { _Pragma("unroll") for (int m = 0; m < 4; ++m) _Pragma("unroll") for (int k = 0; k < 2; ++k) dst[m][k] = *(const PG8_LAS bf16x8*)(lds + PG8_SA(b, h) + aoff + m * 2048 + k * 1024); } while (0)
; #define PG8_LDB(dst, b, h) do { _Pragma("unroll") for (int n = 0; n < 2; ++n) _Pragma("unroll") for (int k = 0; k < 2; ++k) dst[n][k] = *(const PG8_LAS bf16x8*)(lds + PG8_SB(b, h) + boff + n * 2048 + k * 1024); } while (0)
; #define PG8_MMA(ai, bj, At, Bt) do { __builtin_amdgcn_s_setprio(1); _Pragma("unroll") for (int m = 0; m < 4; ++m) _Pragma("unroll") for (int n = 0; n < 2; ++n) _Pragma("unroll") for (int k = 0; k < 2; ++k) \
;         acc[ai][bj][m][n] = __builtin_amdgcn_mfma_f32_16x16x32_bf16(Bt[n][k], At[m][k], acc[ai][bj][m][n], 0, 0, 0); __builtin_amdgcn_s_setprio(0); } while (0)
; #define PG8_WAIT_V(n) asm volatile("s_waitcnt vmcnt(" #n ")" ::: "memory")
; #define PG8_WAIT_L(n) asm volatile("s_waitcnt lgkmcnt(" #n ")" ::: "memory")
; #define PG8_BAR __builtin_amdgcn_s_barrier()
; template <class Epi, class Sched, bool ALIGN_EPI>
; __device__ __forceinline__ void gemm_phase(PG8_LAS unsigned char* lds, const Gemm g, const Sched& S, const Epi& E, const int tid) {
;     ...
;         const bool has_next = S.next(ui + 1, nxt);
;         const char* nA = has_next ? (const char*)g.A + (size_t)nxt.pm * tstepA + PG8_ACOL(nxt) : cA; const char* nB = has_next ? (const char*)g.Bt + (size_t)nxt.pn * tstepB : cB;
;         for (int t = 0; t < nt; t += 2) {
;             const bool last = (t == nt - 2);
;             const char* a1 = cA + (size_t)(t + 1) * kstepA;
;             const char* a2 = last ? nA : cA + (size_t)(t + 2) * kstepA; const char* b2 = last ? nB : cB + (size_t)(t + 2) * kstepB;
;             const char* a3 = a2 + kstepA; const char* b3 = b2 + kstepB;
;             if (last && has_next) S.a_ready(nxt);
;             PG8_LDB(B0, 0, 0); PG8_LDB(B1, 0, 1); PG8_SCHED; PG8_LDA(At, 0, 0); PG8_STAGE(PG8_SA(1, 1), a1 + hstepA, voffA);
;             PG8_WAIT_V(8); PG8_WAIT_L(0); PG8_BAR; PG8_MMA(0, 0, At, B0); PG8_MMA(0, 1, At, B1); PG8_BAR; PG8_SCHED;
.LBB0_341:
	s_ashr_i32 s47, s46, 31
	s_lshl_b64 s[48:49], s[46:47], 20
	s_add_u32 s48, s57, s48
	s_addc_u32 s49, s58, s49
	s_and_b64 s[50:51], s[6:7], exec
	s_cselect_b32 s9, s49, s11
	s_cselect_b32 s43, s48, s10
	s_ashr_i32 s45, s44, 31
	s_lshl_b64 s[50:51], s[44:45], 20
	s_add_u32 s50, s56, s50
	s_addc_u32 s51, s33, s51
	s_and_b64 s[52:53], s[6:7], exec
	s_cselect_b32 s45, s51, s13
	s_cselect_b32 s47, s50, s12
	s_add_u32 s10, s10, 0xc000
	s_addc_u32 s11, s11, 0
	s_add_u32 s79, s12, 0x10000
	s_addc_u32 s80, s13, 0
	s_mov_b32 s81, -2
	s_waitcnt lgkmcnt(0)
	s_waitcnt vmcnt(0)
	v_add_u32_e32 v166, 0x10000, v171
	s_add_u32 s12, s10, 0x4000
	s_addc_u32 s13, s11, 0
	s_cmp_eq_u32 s81, 28
	s_cselect_b32 s54, s43, s12
	s_cselect_b32 s55, s9, s13
	s_cselect_b32 s52, s47, s79
	s_cselect_b32 s53, s45, s80
	s_add_u32 s12, s54, 0x8000
	s_addc_u32 s13, s55, 0
	s_add_i32 s82, 0, 0x10000
	s_add_i32 s84, 0, 0x14000
	ds_read_b128 v[48:51], v166
	ds_read_b128 v[52:55], v166 offset:1024
	ds_read_b128 v[64:67], v166 offset:2048
	ds_read_b128 v[68:71], v166 offset:3072
	ds_read_b128 v[146:149], v166 offset:16384
	ds_read_b128 v[150:153], v166 offset:17408
	ds_read_b128 v[180:183], v166 offset:18432
	ds_read_b128 v[184:187], v166 offset:19456
	s_add_i32 m0, s62, 0xc000
	ds_read_b128 v[188:191], v210
	ds_read_b128 v[192:195], v210 offset:1024
	ds_read_b128 v[196:199], v210 offset:2048
	ds_read_b128 v[200:203], v210 offset:3072
	ds_read_b128 v[204:207], v210 offset:4096
	ds_read_b128 v[212:215], v210 offset:5120
	ds_read_b128 v[216:219], v210 offset:6144
	ds_read_b128 v[220:223], v210 offset:7168
	global_load_lds_dwordx4 v176, s[10:11]
	s_add_i32 m0, s62, 0xe000
	s_nop 0
	global_load_lds_dwordx4 v178, s[10:11]
	s_waitcnt vmcnt(8)
	s_waitcnt lgkmcnt(0)
	s_and_b64 vcc, exec, s[34:35]
	s_cbranch_vccz .Lsprio_1
	s_setprio 1

; #define PG8_STAGE(bufoff, gbase, voff) do { _Pragma("unroll") for (int _i = 0; _i < 2; ++_i) \
;         __builtin_amdgcn_global_load_lds((const unsigned*)((const char*)(gbase) + (voff)[_i]), (PG8_LAS unsigned*)(lds + (bufoff) + ldsw + _i * 8192), 16, 0, 0); } while (0)
; #define PG8_LDA(dst, b, h) do { _Pragma("unroll") for (int m = 0; m < 4; ++m) _Pragma("unroll") for (int k = 0; k < 2; ++k) dst[m][k] = *(const PG8_LAS bf16x8*)(lds + PG8_SA(b, h) + aoff + m * 2048 + k * 1024); } while (0)
; #define PG8_LDB(dst, b, h) do { _Pragma("unroll") for (int n = 0; n < 2; ++n) _Pragma("unroll") for (int k = 0; k < 2; ++k) dst[n][k] = *(const PG8_LAS bf16x8*)(lds + PG8_SB(b, h) + boff + n * 2048 + k * 1024); } while (0)
; #define PG8_MMA(ai, bj, At, Bt) do { __builtin_amdgcn_s_setprio(1); _Pragma("unroll") for (int m = 0; m < 4; ++m) _Pragma("unroll") for (int n = 0; n < 2; ++n) _Pragma("unroll") for (int k = 0; k < 2; ++k) \
;         acc[ai][bj][m][n] = __builtin_amdgcn_mfma_f32_16x16x32_bf16(Bt[n][k], At[m][k], acc[ai][bj][m][n], 0, 0, 0); __builtin_amdgcn_s_setprio(0); } while (0)
; #define PG8_WAIT_V(n) asm volatile("s_waitcnt vmcnt(" #n ")" ::: "memory")
; #define PG8_WAIT_L(n) asm volatile("s_waitcnt lgkmcnt(" #n ")" ::: "memory")
; #define PG8_BAR __builtin_amdgcn_s_barrier()
; template <class Epi, class Sched, bool ALIGN_EPI>
; __device__ __forceinline__ void gemm_phase(PG8_LAS unsigned char* lds, const Gemm g, const Sched& S, const Epi& E, const int tid) {
;     ...
;         const bool has_next = S.next(ui + 1, nxt);
;         const char* nA = has_next ? (const char*)g.A + (size_t)nxt.pm * tstepA + PG8_ACOL(nxt) : cA; const char* nB = has_next ? (const char*)g.Bt + (size_t)nxt.pn * tstepB : cB;
;         for (int t = 0; t < nt; t += 2) {
;             const bool last = (t == nt - 2);
;             const char* a1 = cA + (size_t)(t + 1) * kstepA;
;             const char* a2 = last ? nA : cA + (size_t)(t + 2) * kstepA; const char* b2 = last ? nB : cB + (size_t)(t + 2) * kstepB;
;             const char* a3 = a2 + kstepA; const char* b3 = b2 + kstepB;
;             if (last && has_next) S.a_ready(nxt);
;             PG8_LDB(B0, 0, 0); PG8_LDB(B1, 0, 1); PG8_SCHED; PG8_LDA(At, 0, 0); PG8_STAGE(PG8_SA(1, 1), a1 + hstepA, voffA);
;             PG8_WAIT_V(8); PG8_WAIT_L(0); PG8_BAR; PG8_MMA(0, 0, At, B0); PG8_MMA(0, 1, At, B1); PG8_BAR; PG8_SCHED;
.LBB0_1395:
	s_add_u32 s50, s18, s68
	s_addc_u32 s51, s19, s69
	s_add_u32 s52, s20, 0x10000
	s_addc_u32 s53, s21, 0
	s_mov_b64 s[20:21], 0
	v_add_u32_e32 v192, 0x10000, v195
	s_add_u32 s54, s20, 1
	s_addc_u32 s55, s21, 0
	s_add_u32 s22, s20, 2
	s_addc_u32 s23, s21, 0
	s_lshl_b64 s[24:25], s[22:23], s44
	s_add_u32 s21, s18, s24
	s_addc_u32 s24, s19, s25
	s_cmp_eq_u32 s45, s20
	s_cselect_b32 s26, s8, s21
	s_cselect_b32 s27, s9, s24
	s_cselect_b32 s24, s16, s52
	s_cselect_b32 s25, s17, s53
	s_add_u32 s20, s26, s38
	s_addc_u32 s21, s27, 0
	s_add_i32 s56, 0, 0x10000
	s_add_i32 s57, 0, 0x14000
	ds_read_b128 v[88:91], v192
	ds_read_b128 v[92:95], v192 offset:1024
	ds_read_b128 v[100:103], v192 offset:2048
	ds_read_b128 v[108:111], v192 offset:3072
	ds_read_b128 v[146:149], v192 offset:16384
	ds_read_b128 v[150:153], v192 offset:17408
	ds_read_b128 v[154:157], v192 offset:18432
	ds_read_b128 v[158:161], v192 offset:19456
	s_lshl_b64 s[54:55], s[54:55], s44
	s_add_u32 s54, s50, s54
	s_addc_u32 s55, s51, s55
	s_add_i32 m0, s31, 0xc000
	ds_read_b128 v[162:165], v185
	ds_read_b128 v[166:169], v185 offset:1024
	ds_read_b128 v[172:175], v185 offset:2048
	ds_read_b128 v[188:191], v185 offset:3072
	ds_read_b128 v[196:199], v185 offset:4096
	ds_read_b128 v[200:203], v185 offset:5120
	ds_read_b128 v[204:207], v185 offset:6144
	ds_read_b128 v[208:211], v185 offset:7168
	global_load_lds_dwordx4 v176, s[54:55]
	s_add_i32 m0, s31, 0xe000
	s_nop 0
	global_load_lds_dwordx4 v180, s[54:55]
	s_waitcnt vmcnt(8)
	s_waitcnt lgkmcnt(0)
	s_and_b64 vcc, exec, s[14:15]
	s_cbranch_vccz .Lsprio_2
	s_setprio 1
